# v060 + layer-1 q-projection epilogue: the second rope-table load pair of each row group issued with the first (8 waits per unit instead of 16)
# speedup vs baseline: 1.0003x; 1.0003x over previous
;     __device__ __forceinline__ void operator()(const f32x4 (&acc)[2][2][4][2], const Unit& u, int wr, int wc, int fr, int fq) const {
;     ...
;                     const int row = row0 + ai * HALF + m * 16; const int t = row & (SEQ - 1);
;                     const int pos = wc < 2 ? (t >> 6) : (t & 63);
;                     const f32x4* tp = (const f32x4*)(rope + pos * 64 + (wc & 1) * 32 + 8 * fq);
;                     f32x4 o1[2], o2[2];
; #pragma unroll
;                     for (int n = 0; n < 2; ++n) {
;                         const f32x4 x1 = acc[ai][0][m][n], x2 = acc[ai][1][m][n];
;                         if (lat) { const f32x4 cs0 = tp[2 * n], cs1 = tp[2 * n + 1];
;                             o1[n][0] = (x1[0] * cs0[0] - x2[0] * cs0[1]) * sc; o2[n][0] = (x1[0] * cs0[1] + x2[0] * cs0[0]) * sc;
;                             o1[n][1] = (x1[1] * cs0[2] - x2[1] * cs0[3]) * sc; o2[n][1] = (x1[1] * cs0[3] + x2[1] * cs0[2]) * sc;
;                             o1[n][2] = (x1[2] * cs1[0] - x2[2] * cs1[1]) * sc; o2[n][2] = (x1[2] * cs1[1] + x2[2] * cs1[0]) * sc;
;                             o1[n][3] = (x1[3] * cs1[2] - x2[3] * cs1[3]) * sc; o2[n][3] = (x1[3] * cs1[3] + x2[3] * cs1[2]) * sc;
.LBB0_1266:
	v_bfe_u32 v157, v156, 6, 7
	v_cndmask_b32_e64 v142, v1, v157, s[6:7]
	v_lshlrev_b32_e32 v142, 9, v142
	s_andn2_b64 vcc, exec, s[10:11]
	v_lshl_add_u64 v[168:169], v[146:147], 0, v[142:143]
	s_cbranch_vccnz .LBB0_1268
	global_load_dwordx4 v[160:163], v[168:169], off
	global_load_dwordx4 v[164:167], v[168:169], off offset:16
	global_load_dwordx4 v[232:235], v[168:169], off offset:32
	global_load_dwordx4 v[236:239], v[168:169], off offset:48
	s_waitcnt vmcnt(2)
	v_mov_b32_e32 v192, v160
	v_mov_b32_e32 v193, v162
	v_mov_b32_e32 v162, v161
	v_mul_f32_e32 v194, v128, v164
	v_mul_f32_e32 v196, v124, v165
	v_mul_f32_e32 v200, v128, v165
	v_mul_f32_e32 v202, v124, v164
	v_mov_b32_e32 v124, v129
	v_mov_b32_e32 v128, v125
	v_pk_mul_f32 v[160:161], v[122:123], v[162:163]
	v_pk_mul_f32 v[122:123], v[122:123], v[192:193]
	v_pk_mul_f32 v[124:125], v[124:125], v[166:167]
	v_pk_mul_f32 v[128:129], v[128:129], v[166:167]
	v_pk_fma_f32 v[160:161], v[126:127], v[192:193], v[160:161] neg_lo:[0,0,1] neg_hi:[0,0,1]
	v_pk_fma_f32 v[122:123], v[126:127], v[162:163], v[122:123]
	v_mov_b32_e32 v195, v124
	v_mov_b32_e32 v197, v125
	v_mov_b32_e32 v201, v129
	v_mov_b32_e32 v203, v128
	v_pk_mul_f32 v[164:165], v[158:159], v[160:161] op_sel_hi:[0,1]
	v_pk_mul_f32 v[160:161], v[158:159], v[122:123] op_sel_hi:[0,1]
	v_pk_add_f32 v[122:123], v[194:195], v[196:197] neg_lo:[0,1] neg_hi:[0,1]
	v_pk_add_f32 v[124:125], v[200:201], v[202:203]
	v_pk_mul_f32 v[166:167], v[158:159], v[122:123] op_sel_hi:[0,1]
	v_pk_mul_f32 v[162:163], v[158:159], v[124:125] op_sel_hi:[0,1]

;     __device__ __forceinline__ void operator()(const f32x4 (&acc)[2][2][4][2], const Unit& u, int wr, int wc, int fr, int fq) const {
;     ...
;                     for (int n = 0; n < 2; ++n) {
;                         const f32x4 x1 = acc[ai][0][m][n], x2 = acc[ai][1][m][n];
;                         if (lat) { const f32x4 cs0 = tp[2 * n], cs1 = tp[2 * n + 1];
;                             o1[n][0] = (x1[0] * cs0[0] - x2[0] * cs0[1]) * sc; o2[n][0] = (x1[0] * cs0[1] + x2[0] * cs0[0]) * sc;
;                             o1[n][1] = (x1[1] * cs0[2] - x2[1] * cs0[3]) * sc; o2[n][1] = (x1[1] * cs0[3] + x2[1] * cs0[2]) * sc;
;                             o1[n][2] = (x1[2] * cs1[0] - x2[2] * cs1[1]) * sc; o2[n][2] = (x1[2] * cs1[1] + x2[2] * cs1[0]) * sc;
;                             o1[n][3] = (x1[3] * cs1[2] - x2[3] * cs1[3]) * sc; o2[n][3] = (x1[3] * cs1[3] + x2[3] * cs1[2]) * sc;
;                         } else { o1[n] = x1 * sc; o2[n] = x2 * sc; }
.LBB0_1270:
	s_andn2_b64 vcc, exec, s[40:41]
	s_cbranch_vccnz .LBB0_1272
	s_waitcnt vmcnt(0)
	v_mov_b32_e32 v122, v232
	v_mov_b32_e32 v123, v233
	v_mov_b32_e32 v124, v234
	v_mov_b32_e32 v125, v235
	v_mov_b32_e32 v126, v236
	v_mov_b32_e32 v127, v237
	v_mov_b32_e32 v128, v238
	v_mov_b32_e32 v129, v239
	v_mov_b32_e32 v168, v122
	v_mov_b32_e32 v169, v124
	v_mov_b32_e32 v124, v123
	v_mul_f32_e32 v122, v120, v126
	v_mul_f32_e32 v192, v116, v127
	v_mul_f32_e32 v194, v120, v127
	v_mul_f32_e32 v196, v116, v126
	v_mov_b32_e32 v116, v121
	v_mov_b32_e32 v120, v117
	v_pk_mul_f32 v[126:127], v[114:115], v[124:125]
	v_pk_mul_f32 v[114:115], v[114:115], v[168:169]
	v_pk_mul_f32 v[116:117], v[116:117], v[128:129]
	v_pk_mul_f32 v[120:121], v[120:121], v[128:129]
	v_pk_fma_f32 v[126:127], v[118:119], v[168:169], v[126:127] neg_lo:[0,0,1] neg_hi:[0,0,1]
	v_pk_fma_f32 v[114:115], v[118:119], v[124:125], v[114:115]
	v_mov_b32_e32 v123, v116
	v_mov_b32_e32 v193, v117
	v_mov_b32_e32 v195, v121
	v_mov_b32_e32 v197, v120
	v_pk_mul_f32 v[128:129], v[158:159], v[126:127] op_sel_hi:[0,1]
	v_pk_mul_f32 v[126:127], v[158:159], v[114:115] op_sel_hi:[0,1]
	v_pk_add_f32 v[114:115], v[122:123], v[192:193] neg_lo:[0,1] neg_hi:[0,1]
	v_pk_add_f32 v[116:117], v[194:195], v[196:197]
	v_pk_mul_f32 v[122:123], v[158:159], v[114:115] op_sel_hi:[0,1]
	v_pk_mul_f32 v[124:125], v[158:159], v[116:117] op_sel_hi:[0,1]

;     __device__ __forceinline__ void operator()(const f32x4 (&acc)[2][2][4][2], const Unit& u, int wr, int wc, int fr, int fq) const {
;     ...
;                     const int row = row0 + ai * HALF + m * 16; const int t = row & (SEQ - 1);
;                     const int pos = wc < 2 ? (t >> 6) : (t & 63);
;                     const f32x4* tp = (const f32x4*)(rope + pos * 64 + (wc & 1) * 32 + 8 * fq);
;                     f32x4 o1[2], o2[2];
; #pragma unroll
;                     for (int n = 0; n < 2; ++n) {
;                         const f32x4 x1 = acc[ai][0][m][n], x2 = acc[ai][1][m][n];
;                         if (lat) { const f32x4 cs0 = tp[2 * n], cs1 = tp[2 * n + 1];
;                             o1[n][0] = (x1[0] * cs0[0] - x2[0] * cs0[1]) * sc; o2[n][0] = (x1[0] * cs0[1] + x2[0] * cs0[0]) * sc;
;                             o1[n][1] = (x1[1] * cs0[2] - x2[1] * cs0[3]) * sc; o2[n][1] = (x1[1] * cs0[3] + x2[1] * cs0[2]) * sc;
;                             o1[n][2] = (x1[2] * cs1[0] - x2[2] * cs1[1]) * sc; o2[n][2] = (x1[2] * cs1[1] + x2[2] * cs1[0]) * sc;
;                             o1[n][3] = (x1[3] * cs1[2] - x2[3] * cs1[3]) * sc; o2[n][3] = (x1[3] * cs1[3] + x2[3] * cs1[2]) * sc;
.LBB0_1274:
	v_cndmask_b32_e64 v124, v171, v157, s[6:7]
	v_lshlrev_b32_e32 v142, 9, v124
	s_andn2_b64 vcc, exec, s[38:39]
	v_lshl_add_u64 v[124:125], v[146:147], 0, v[142:143]
	s_cbranch_vccnz .LBB0_1276
	global_load_dwordx4 v[116:119], v[124:125], off
	global_load_dwordx4 v[120:123], v[124:125], off offset:16
	global_load_dwordx4 v[232:235], v[124:125], off offset:32
	global_load_dwordx4 v[236:239], v[124:125], off offset:48
	s_waitcnt vmcnt(2)
	v_mov_b32_e32 v126, v116
	v_mov_b32_e32 v127, v118
	v_mov_b32_e32 v118, v117
	v_mul_f32_e32 v116, v112, v120
	v_mul_f32_e32 v128, v108, v121
	v_mul_f32_e32 v160, v112, v121
	v_mul_f32_e32 v120, v108, v120
	v_mov_b32_e32 v108, v113
	v_mov_b32_e32 v112, v109
	v_pk_mul_f32 v[162:163], v[106:107], v[118:119]
	v_pk_mul_f32 v[106:107], v[106:107], v[126:127]
	v_pk_mul_f32 v[108:109], v[108:109], v[122:123]
	v_pk_mul_f32 v[112:113], v[112:113], v[122:123]
	v_pk_fma_f32 v[106:107], v[110:111], v[118:119], v[106:107]
	v_mov_b32_e32 v117, v108
	v_mov_b32_e32 v129, v109
	v_mov_b32_e32 v161, v113
	v_mov_b32_e32 v121, v112
	v_pk_fma_f32 v[122:123], v[110:111], v[126:127], v[162:163] neg_lo:[0,0,1] neg_hi:[0,0,1]
	v_pk_mul_f32 v[118:119], v[158:159], v[106:107] op_sel_hi:[0,1]
	v_pk_add_f32 v[106:107], v[116:117], v[128:129] neg_lo:[0,1] neg_hi:[0,1]
	v_pk_add_f32 v[108:109], v[160:161], v[120:121]
	v_pk_mul_f32 v[122:123], v[158:159], v[122:123] op_sel_hi:[0,1]
	v_pk_mul_f32 v[120:121], v[158:159], v[106:107] op_sel_hi:[0,1]
	v_pk_mul_f32 v[116:117], v[158:159], v[108:109] op_sel_hi:[0,1]

;     __device__ __forceinline__ void operator()(const f32x4 (&acc)[2][2][4][2], const Unit& u, int wr, int wc, int fr, int fq) const {
;     ...
;                     for (int n = 0; n < 2; ++n) {
;                         const f32x4 x1 = acc[ai][0][m][n], x2 = acc[ai][1][m][n];
;                         if (lat) { const f32x4 cs0 = tp[2 * n], cs1 = tp[2 * n + 1];
;                             o1[n][0] = (x1[0] * cs0[0] - x2[0] * cs0[1]) * sc; o2[n][0] = (x1[0] * cs0[1] + x2[0] * cs0[0]) * sc;
;                             o1[n][1] = (x1[1] * cs0[2] - x2[1] * cs0[3]) * sc; o2[n][1] = (x1[1] * cs0[3] + x2[1] * cs0[2]) * sc;
;                             o1[n][2] = (x1[2] * cs1[0] - x2[2] * cs1[1]) * sc; o2[n][2] = (x1[2] * cs1[1] + x2[2] * cs1[0]) * sc;
;                             o1[n][3] = (x1[3] * cs1[2] - x2[3] * cs1[3]) * sc; o2[n][3] = (x1[3] * cs1[3] + x2[3] * cs1[2]) * sc;
;                         } else { o1[n] = x1 * sc; o2[n] = x2 * sc; }
.LBB0_1279:
	s_waitcnt vmcnt(0)
	v_mov_b32_e32 v106, v232
	v_mov_b32_e32 v107, v233
	v_mov_b32_e32 v108, v234
	v_mov_b32_e32 v109, v235
	v_mov_b32_e32 v110, v236
	v_mov_b32_e32 v111, v237
	v_mov_b32_e32 v112, v238
	v_mov_b32_e32 v113, v239
	v_mov_b32_e32 v124, v106
	v_mov_b32_e32 v125, v108
	v_mov_b32_e32 v108, v107
	v_mul_f32_e32 v106, v104, v110
	v_mul_f32_e32 v126, v100, v111
	v_mul_f32_e32 v128, v104, v111
	v_mul_f32_e32 v160, v100, v110
	v_mov_b32_e32 v100, v105
	v_mov_b32_e32 v104, v101
	v_pk_mul_f32 v[110:111], v[98:99], v[108:109]
	v_pk_mul_f32 v[98:99], v[98:99], v[124:125]
	v_pk_mul_f32 v[100:101], v[100:101], v[112:113]
	v_pk_mul_f32 v[104:105], v[104:105], v[112:113]
	v_pk_fma_f32 v[110:111], v[102:103], v[124:125], v[110:111] neg_lo:[0,0,1] neg_hi:[0,0,1]
	v_pk_fma_f32 v[98:99], v[102:103], v[108:109], v[98:99]
	v_mov_b32_e32 v107, v100
	v_mov_b32_e32 v127, v101
	v_mov_b32_e32 v129, v105
	v_mov_b32_e32 v161, v104
	v_pk_mul_f32 v[112:113], v[158:159], v[110:111] op_sel_hi:[0,1]
	v_pk_mul_f32 v[110:111], v[158:159], v[98:99] op_sel_hi:[0,1]
	v_pk_add_f32 v[98:99], v[106:107], v[126:127] neg_lo:[0,1] neg_hi:[0,1]
	v_pk_add_f32 v[100:101], v[128:129], v[160:161]
	v_pk_mul_f32 v[106:107], v[158:159], v[98:99] op_sel_hi:[0,1]
	v_pk_mul_f32 v[108:109], v[158:159], v[100:101] op_sel_hi:[0,1]

;     __device__ __forceinline__ void operator()(const f32x4 (&acc)[2][2][4][2], const Unit& u, int wr, int wc, int fr, int fq) const {
;     ...
;                     const int row = row0 + ai * HALF + m * 16; const int t = row & (SEQ - 1);
;                     const int pos = wc < 2 ? (t >> 6) : (t & 63);
;                     const f32x4* tp = (const f32x4*)(rope + pos * 64 + (wc & 1) * 32 + 8 * fq);
;                     f32x4 o1[2], o2[2];
; #pragma unroll
;                     for (int n = 0; n < 2; ++n) {
;                         const f32x4 x1 = acc[ai][0][m][n], x2 = acc[ai][1][m][n];
;                         if (lat) { const f32x4 cs0 = tp[2 * n], cs1 = tp[2 * n + 1];
;                             o1[n][0] = (x1[0] * cs0[0] - x2[0] * cs0[1]) * sc; o2[n][0] = (x1[0] * cs0[1] + x2[0] * cs0[0]) * sc;
;                             o1[n][1] = (x1[1] * cs0[2] - x2[1] * cs0[3]) * sc; o2[n][1] = (x1[1] * cs0[3] + x2[1] * cs0[2]) * sc;
;                             o1[n][2] = (x1[2] * cs1[0] - x2[2] * cs1[1]) * sc; o2[n][2] = (x1[2] * cs1[1] + x2[2] * cs1[0]) * sc;
;                             o1[n][3] = (x1[3] * cs1[2] - x2[3] * cs1[3]) * sc; o2[n][3] = (x1[3] * cs1[3] + x2[3] * cs1[2]) * sc;
.LBB0_1282:
	v_cndmask_b32_e64 v106, v172, v157, s[6:7]
	v_lshlrev_b32_e32 v142, 9, v106
	s_andn2_b64 vcc, exec, s[38:39]
	v_lshl_add_u64 v[106:107], v[146:147], 0, v[142:143]
	s_cbranch_vccnz .LBB0_1284
	global_load_dwordx4 v[98:101], v[106:107], off
	global_load_dwordx4 v[102:105], v[106:107], off offset:16
	global_load_dwordx4 v[232:235], v[106:107], off offset:32
	global_load_dwordx4 v[236:239], v[106:107], off offset:48
	s_waitcnt vmcnt(2)
	v_mov_b32_e32 v108, v98
	v_mov_b32_e32 v109, v100
	v_mov_b32_e32 v100, v99
	v_mul_f32_e32 v98, v96, v102
	v_mul_f32_e32 v110, v92, v103
	v_mul_f32_e32 v112, v96, v103
	v_mul_f32_e32 v102, v92, v102
	v_mov_b32_e32 v92, v97
	v_mov_b32_e32 v96, v93
	v_pk_mul_f32 v[116:117], v[90:91], v[100:101]
	v_pk_mul_f32 v[90:91], v[90:91], v[108:109]
	v_pk_mul_f32 v[92:93], v[92:93], v[104:105]
	v_pk_mul_f32 v[96:97], v[96:97], v[104:105]
	v_pk_fma_f32 v[90:91], v[94:95], v[100:101], v[90:91]
	v_mov_b32_e32 v99, v92
	v_mov_b32_e32 v111, v93
	v_mov_b32_e32 v113, v97
	v_mov_b32_e32 v103, v96
	v_pk_fma_f32 v[104:105], v[94:95], v[108:109], v[116:117] neg_lo:[0,0,1] neg_hi:[0,0,1]
	v_pk_mul_f32 v[100:101], v[158:159], v[90:91] op_sel_hi:[0,1]
	v_pk_add_f32 v[90:91], v[98:99], v[110:111] neg_lo:[0,1] neg_hi:[0,1]
	v_pk_add_f32 v[92:93], v[112:113], v[102:103]
	v_pk_mul_f32 v[104:105], v[158:159], v[104:105] op_sel_hi:[0,1]
	v_pk_mul_f32 v[102:103], v[158:159], v[90:91] op_sel_hi:[0,1]
	v_pk_mul_f32 v[98:99], v[158:159], v[92:93] op_sel_hi:[0,1]

;     __device__ __forceinline__ void operator()(const f32x4 (&acc)[2][2][4][2], const Unit& u, int wr, int wc, int fr, int fq) const {
;     ...
;                     for (int n = 0; n < 2; ++n) {
;                         const f32x4 x1 = acc[ai][0][m][n], x2 = acc[ai][1][m][n];
;                         if (lat) { const f32x4 cs0 = tp[2 * n], cs1 = tp[2 * n + 1];
;                             o1[n][0] = (x1[0] * cs0[0] - x2[0] * cs0[1]) * sc; o2[n][0] = (x1[0] * cs0[1] + x2[0] * cs0[0]) * sc;
;                             o1[n][1] = (x1[1] * cs0[2] - x2[1] * cs0[3]) * sc; o2[n][1] = (x1[1] * cs0[3] + x2[1] * cs0[2]) * sc;
;                             o1[n][2] = (x1[2] * cs1[0] - x2[2] * cs1[1]) * sc; o2[n][2] = (x1[2] * cs1[1] + x2[2] * cs1[0]) * sc;
;                             o1[n][3] = (x1[3] * cs1[2] - x2[3] * cs1[3]) * sc; o2[n][3] = (x1[3] * cs1[3] + x2[3] * cs1[2]) * sc;
;                         } else { o1[n] = x1 * sc; o2[n] = x2 * sc; }
.LBB0_1287:
	s_waitcnt vmcnt(0)
	v_mov_b32_e32 v90, v232
	v_mov_b32_e32 v91, v233
	v_mov_b32_e32 v92, v234
	v_mov_b32_e32 v93, v235
	v_mov_b32_e32 v94, v236
	v_mov_b32_e32 v95, v237
	v_mov_b32_e32 v96, v238
	v_mov_b32_e32 v97, v239
	v_mov_b32_e32 v106, v90
	v_mov_b32_e32 v107, v92
	v_mov_b32_e32 v92, v91
	v_mul_f32_e32 v90, v88, v94
	v_mul_f32_e32 v108, v84, v95
	v_mul_f32_e32 v110, v88, v95
	v_mul_f32_e32 v112, v84, v94
	v_mov_b32_e32 v84, v89
	v_mov_b32_e32 v88, v85
	v_pk_mul_f32 v[94:95], v[82:83], v[92:93]
	v_pk_mul_f32 v[82:83], v[82:83], v[106:107]
	v_pk_mul_f32 v[84:85], v[84:85], v[96:97]
	v_pk_mul_f32 v[88:89], v[88:89], v[96:97]
	v_pk_fma_f32 v[94:95], v[86:87], v[106:107], v[94:95] neg_lo:[0,0,1] neg_hi:[0,0,1]
	v_pk_fma_f32 v[82:83], v[86:87], v[92:93], v[82:83]
	v_mov_b32_e32 v91, v84
	v_mov_b32_e32 v109, v85
	v_mov_b32_e32 v111, v89
	v_mov_b32_e32 v113, v88
	v_pk_mul_f32 v[96:97], v[158:159], v[94:95] op_sel_hi:[0,1]
	v_pk_mul_f32 v[94:95], v[158:159], v[82:83] op_sel_hi:[0,1]
	v_pk_add_f32 v[82:83], v[90:91], v[108:109] neg_lo:[0,1] neg_hi:[0,1]
	v_pk_add_f32 v[84:85], v[110:111], v[112:113]
	v_pk_mul_f32 v[90:91], v[158:159], v[82:83] op_sel_hi:[0,1]
	v_pk_mul_f32 v[92:93], v[158:159], v[84:85] op_sel_hi:[0,1]

;     __device__ __forceinline__ void operator()(const f32x4 (&acc)[2][2][4][2], const Unit& u, int wr, int wc, int fr, int fq) const {
;     ...
;                     const int row = row0 + ai * HALF + m * 16; const int t = row & (SEQ - 1);
;                     const int pos = wc < 2 ? (t >> 6) : (t & 63);
;                     const f32x4* tp = (const f32x4*)(rope + pos * 64 + (wc & 1) * 32 + 8 * fq);
;                     f32x4 o1[2], o2[2];
; #pragma unroll
;                     for (int n = 0; n < 2; ++n) {
;                         const f32x4 x1 = acc[ai][0][m][n], x2 = acc[ai][1][m][n];
;                         if (lat) { const f32x4 cs0 = tp[2 * n], cs1 = tp[2 * n + 1];
;                             o1[n][0] = (x1[0] * cs0[0] - x2[0] * cs0[1]) * sc; o2[n][0] = (x1[0] * cs0[1] + x2[0] * cs0[0]) * sc;
;                             o1[n][1] = (x1[1] * cs0[2] - x2[1] * cs0[3]) * sc; o2[n][1] = (x1[1] * cs0[3] + x2[1] * cs0[2]) * sc;
;                             o1[n][2] = (x1[2] * cs1[0] - x2[2] * cs1[1]) * sc; o2[n][2] = (x1[2] * cs1[1] + x2[2] * cs1[0]) * sc;
;                             o1[n][3] = (x1[3] * cs1[2] - x2[3] * cs1[3]) * sc; o2[n][3] = (x1[3] * cs1[3] + x2[3] * cs1[2]) * sc;
.LBB0_1290:
	v_cndmask_b32_e64 v90, v173, v157, s[6:7]
	v_lshlrev_b32_e32 v142, 9, v90
	s_andn2_b64 vcc, exec, s[38:39]
	v_lshl_add_u64 v[90:91], v[146:147], 0, v[142:143]
	s_cbranch_vccnz .LBB0_1292
	global_load_dwordx4 v[82:85], v[90:91], off
	global_load_dwordx4 v[86:89], v[90:91], off offset:16
	global_load_dwordx4 v[232:235], v[90:91], off offset:32
	global_load_dwordx4 v[236:239], v[90:91], off offset:48
	s_waitcnt vmcnt(2)
	v_mov_b32_e32 v92, v82
	v_mov_b32_e32 v93, v84
	v_mov_b32_e32 v84, v83
	v_mul_f32_e32 v82, v80, v86
	v_mul_f32_e32 v94, v76, v87
	v_mul_f32_e32 v96, v80, v87
	v_mul_f32_e32 v86, v76, v86
	v_mov_b32_e32 v76, v81
	v_mov_b32_e32 v80, v77
	v_pk_mul_f32 v[98:99], v[74:75], v[84:85]
	v_pk_mul_f32 v[74:75], v[74:75], v[92:93]
	v_pk_mul_f32 v[76:77], v[76:77], v[88:89]
	v_pk_mul_f32 v[80:81], v[80:81], v[88:89]
	v_pk_fma_f32 v[74:75], v[78:79], v[84:85], v[74:75]
	v_mov_b32_e32 v83, v76
	v_mov_b32_e32 v95, v77
	v_mov_b32_e32 v97, v81
	v_mov_b32_e32 v87, v80
	v_pk_fma_f32 v[88:89], v[78:79], v[92:93], v[98:99] neg_lo:[0,0,1] neg_hi:[0,0,1]
	v_pk_mul_f32 v[84:85], v[158:159], v[74:75] op_sel_hi:[0,1]
	v_pk_add_f32 v[74:75], v[82:83], v[94:95] neg_lo:[0,1] neg_hi:[0,1]
	v_pk_add_f32 v[76:77], v[96:97], v[86:87]
	v_pk_mul_f32 v[88:89], v[158:159], v[88:89] op_sel_hi:[0,1]
	v_pk_mul_f32 v[86:87], v[158:159], v[74:75] op_sel_hi:[0,1]
	v_pk_mul_f32 v[82:83], v[158:159], v[76:77] op_sel_hi:[0,1]

;     __device__ __forceinline__ void operator()(const f32x4 (&acc)[2][2][4][2], const Unit& u, int wr, int wc, int fr, int fq) const {
;     ...
;                     for (int n = 0; n < 2; ++n) {
;                         const f32x4 x1 = acc[ai][0][m][n], x2 = acc[ai][1][m][n];
;                         if (lat) { const f32x4 cs0 = tp[2 * n], cs1 = tp[2 * n + 1];
;                             o1[n][0] = (x1[0] * cs0[0] - x2[0] * cs0[1]) * sc; o2[n][0] = (x1[0] * cs0[1] + x2[0] * cs0[0]) * sc;
;                             o1[n][1] = (x1[1] * cs0[2] - x2[1] * cs0[3]) * sc; o2[n][1] = (x1[1] * cs0[3] + x2[1] * cs0[2]) * sc;
;                             o1[n][2] = (x1[2] * cs1[0] - x2[2] * cs1[1]) * sc; o2[n][2] = (x1[2] * cs1[1] + x2[2] * cs1[0]) * sc;
;                             o1[n][3] = (x1[3] * cs1[2] - x2[3] * cs1[3]) * sc; o2[n][3] = (x1[3] * cs1[3] + x2[3] * cs1[2]) * sc;
;                         } else { o1[n] = x1 * sc; o2[n] = x2 * sc; }
.LBB0_1295:
	s_waitcnt vmcnt(0)
	v_mov_b32_e32 v74, v232
	v_mov_b32_e32 v75, v233
	v_mov_b32_e32 v76, v234
	v_mov_b32_e32 v77, v235
	v_mov_b32_e32 v78, v236
	v_mov_b32_e32 v79, v237
	v_mov_b32_e32 v80, v238
	v_mov_b32_e32 v81, v239
	v_mov_b32_e32 v90, v74
	v_mov_b32_e32 v91, v76
	v_mov_b32_e32 v76, v75
	v_mul_f32_e32 v74, v72, v78
	v_mul_f32_e32 v92, v68, v79
	v_mul_f32_e32 v94, v72, v79
	v_mul_f32_e32 v96, v68, v78
	v_mov_b32_e32 v68, v73
	v_mov_b32_e32 v72, v69
	v_pk_mul_f32 v[78:79], v[66:67], v[76:77]
	v_pk_mul_f32 v[66:67], v[66:67], v[90:91]
	v_pk_mul_f32 v[68:69], v[68:69], v[80:81]
	v_pk_mul_f32 v[72:73], v[72:73], v[80:81]
	v_pk_fma_f32 v[78:79], v[70:71], v[90:91], v[78:79] neg_lo:[0,0,1] neg_hi:[0,0,1]
	v_pk_fma_f32 v[66:67], v[70:71], v[76:77], v[66:67]
	v_mov_b32_e32 v75, v68
	v_mov_b32_e32 v93, v69
	v_mov_b32_e32 v95, v73
	v_mov_b32_e32 v97, v72
	v_pk_mul_f32 v[80:81], v[158:159], v[78:79] op_sel_hi:[0,1]
	v_pk_mul_f32 v[78:79], v[158:159], v[66:67] op_sel_hi:[0,1]
	v_pk_add_f32 v[66:67], v[74:75], v[92:93] neg_lo:[0,1] neg_hi:[0,1]
	v_pk_add_f32 v[68:69], v[94:95], v[96:97]
	v_pk_mul_f32 v[74:75], v[158:159], v[66:67] op_sel_hi:[0,1]
	v_pk_mul_f32 v[76:77], v[158:159], v[68:69] op_sel_hi:[0,1]

;     __device__ __forceinline__ void operator()(const f32x4 (&acc)[2][2][4][2], const Unit& u, int wr, int wc, int fr, int fq) const {
;     ...
;                     const int row = row0 + ai * HALF + m * 16; const int t = row & (SEQ - 1);
;                     const int pos = wc < 2 ? (t >> 6) : (t & 63);
;                     const f32x4* tp = (const f32x4*)(rope + pos * 64 + (wc & 1) * 32 + 8 * fq);
;                     f32x4 o1[2], o2[2];
; #pragma unroll
;                     for (int n = 0; n < 2; ++n) {
;                         const f32x4 x1 = acc[ai][0][m][n], x2 = acc[ai][1][m][n];
;                         if (lat) { const f32x4 cs0 = tp[2 * n], cs1 = tp[2 * n + 1];
;                             o1[n][0] = (x1[0] * cs0[0] - x2[0] * cs0[1]) * sc; o2[n][0] = (x1[0] * cs0[1] + x2[0] * cs0[0]) * sc;
;                             o1[n][1] = (x1[1] * cs0[2] - x2[1] * cs0[3]) * sc; o2[n][1] = (x1[1] * cs0[3] + x2[1] * cs0[2]) * sc;
;                             o1[n][2] = (x1[2] * cs1[0] - x2[2] * cs1[1]) * sc; o2[n][2] = (x1[2] * cs1[1] + x2[2] * cs1[0]) * sc;
;                             o1[n][3] = (x1[3] * cs1[2] - x2[3] * cs1[3]) * sc; o2[n][3] = (x1[3] * cs1[3] + x2[3] * cs1[2]) * sc;
.LBB0_1298:
	v_add_u32_e32 v76, 0x80, v156
	v_bfe_u32 v74, v76, 6, 7
	v_cndmask_b32_e64 v74, v1, v74, s[6:7]
	v_lshlrev_b32_e32 v142, 9, v74
	s_andn2_b64 vcc, exec, s[38:39]
	v_lshl_add_u64 v[74:75], v[146:147], 0, v[142:143]
	s_cbranch_vccnz .LBB0_1300
	global_load_dwordx4 v[66:69], v[74:75], off
	global_load_dwordx4 v[70:73], v[74:75], off offset:16
	global_load_dwordx4 v[232:235], v[74:75], off offset:32
	global_load_dwordx4 v[236:239], v[74:75], off offset:48
	s_waitcnt vmcnt(2)
	v_mov_b32_e32 v78, v66
	v_mov_b32_e32 v79, v68
	v_mov_b32_e32 v68, v67
	v_mul_f32_e32 v66, v64, v70
	v_mul_f32_e32 v80, v60, v71
	v_mul_f32_e32 v82, v64, v71
	v_mul_f32_e32 v70, v60, v70
	v_mov_b32_e32 v60, v65
	v_mov_b32_e32 v64, v61
	v_pk_mul_f32 v[84:85], v[58:59], v[68:69]
	v_pk_mul_f32 v[58:59], v[58:59], v[78:79]
	v_pk_mul_f32 v[60:61], v[60:61], v[72:73]
	v_pk_mul_f32 v[64:65], v[64:65], v[72:73]
	v_pk_fma_f32 v[58:59], v[62:63], v[68:69], v[58:59]
	v_mov_b32_e32 v67, v60
	v_mov_b32_e32 v81, v61
	v_mov_b32_e32 v83, v65
	v_mov_b32_e32 v71, v64
	v_pk_fma_f32 v[72:73], v[62:63], v[78:79], v[84:85] neg_lo:[0,0,1] neg_hi:[0,0,1]
	v_pk_mul_f32 v[68:69], v[158:159], v[58:59] op_sel_hi:[0,1]
	v_pk_add_f32 v[58:59], v[66:67], v[80:81] neg_lo:[0,1] neg_hi:[0,1]
	v_pk_add_f32 v[60:61], v[82:83], v[70:71]
	v_pk_mul_f32 v[72:73], v[158:159], v[72:73] op_sel_hi:[0,1]
	v_pk_mul_f32 v[70:71], v[158:159], v[58:59] op_sel_hi:[0,1]
	v_pk_mul_f32 v[66:67], v[158:159], v[60:61] op_sel_hi:[0,1]

;     __device__ __forceinline__ void operator()(const f32x4 (&acc)[2][2][4][2], const Unit& u, int wr, int wc, int fr, int fq) const {
;     ...
;                     for (int n = 0; n < 2; ++n) {
;                         const f32x4 x1 = acc[ai][0][m][n], x2 = acc[ai][1][m][n];
;                         if (lat) { const f32x4 cs0 = tp[2 * n], cs1 = tp[2 * n + 1];
;                             o1[n][0] = (x1[0] * cs0[0] - x2[0] * cs0[1]) * sc; o2[n][0] = (x1[0] * cs0[1] + x2[0] * cs0[0]) * sc;
;                             o1[n][1] = (x1[1] * cs0[2] - x2[1] * cs0[3]) * sc; o2[n][1] = (x1[1] * cs0[3] + x2[1] * cs0[2]) * sc;
;                             o1[n][2] = (x1[2] * cs1[0] - x2[2] * cs1[1]) * sc; o2[n][2] = (x1[2] * cs1[1] + x2[2] * cs1[0]) * sc;
;                             o1[n][3] = (x1[3] * cs1[2] - x2[3] * cs1[3]) * sc; o2[n][3] = (x1[3] * cs1[3] + x2[3] * cs1[2]) * sc;
;                         } else { o1[n] = x1 * sc; o2[n] = x2 * sc; }
.LBB0_1303:
	s_waitcnt vmcnt(0)
	v_mov_b32_e32 v58, v232
	v_mov_b32_e32 v59, v233
	v_mov_b32_e32 v60, v234
	v_mov_b32_e32 v61, v235
	v_mov_b32_e32 v62, v236
	v_mov_b32_e32 v63, v237
	v_mov_b32_e32 v64, v238
	v_mov_b32_e32 v65, v239
	v_mov_b32_e32 v74, v58
	v_mov_b32_e32 v75, v60
	v_mov_b32_e32 v60, v59
	v_mul_f32_e32 v58, v56, v62
	v_mul_f32_e32 v78, v52, v63
	v_mul_f32_e32 v80, v56, v63
	v_mul_f32_e32 v82, v52, v62
	v_mov_b32_e32 v52, v57
	v_mov_b32_e32 v56, v53
	v_pk_mul_f32 v[62:63], v[50:51], v[60:61]
	v_pk_mul_f32 v[50:51], v[50:51], v[74:75]
	v_pk_mul_f32 v[52:53], v[52:53], v[64:65]
	v_pk_mul_f32 v[56:57], v[56:57], v[64:65]
	v_pk_fma_f32 v[62:63], v[54:55], v[74:75], v[62:63] neg_lo:[0,0,1] neg_hi:[0,0,1]
	v_pk_fma_f32 v[50:51], v[54:55], v[60:61], v[50:51]
	v_mov_b32_e32 v59, v52
	v_mov_b32_e32 v79, v53
	v_mov_b32_e32 v81, v57
	v_mov_b32_e32 v83, v56
	v_pk_mul_f32 v[64:65], v[158:159], v[62:63] op_sel_hi:[0,1]
	v_pk_mul_f32 v[62:63], v[158:159], v[50:51] op_sel_hi:[0,1]
	v_pk_add_f32 v[50:51], v[58:59], v[78:79] neg_lo:[0,1] neg_hi:[0,1]
	v_pk_add_f32 v[52:53], v[80:81], v[82:83]
	v_pk_mul_f32 v[58:59], v[158:159], v[50:51] op_sel_hi:[0,1]
	v_pk_mul_f32 v[60:61], v[158:159], v[52:53] op_sel_hi:[0,1]

;     __device__ __forceinline__ void operator()(const f32x4 (&acc)[2][2][4][2], const Unit& u, int wr, int wc, int fr, int fq) const {
;     ...
;                     const int row = row0 + ai * HALF + m * 16; const int t = row & (SEQ - 1);
;                     const int pos = wc < 2 ? (t >> 6) : (t & 63);
;                     const f32x4* tp = (const f32x4*)(rope + pos * 64 + (wc & 1) * 32 + 8 * fq);
;                     f32x4 o1[2], o2[2];
; #pragma unroll
;                     for (int n = 0; n < 2; ++n) {
;                         const f32x4 x1 = acc[ai][0][m][n], x2 = acc[ai][1][m][n];
;                         if (lat) { const f32x4 cs0 = tp[2 * n], cs1 = tp[2 * n + 1];
;                             o1[n][0] = (x1[0] * cs0[0] - x2[0] * cs0[1]) * sc; o2[n][0] = (x1[0] * cs0[1] + x2[0] * cs0[0]) * sc;
;                             o1[n][1] = (x1[1] * cs0[2] - x2[1] * cs0[3]) * sc; o2[n][1] = (x1[1] * cs0[3] + x2[1] * cs0[2]) * sc;
;                             o1[n][2] = (x1[2] * cs1[0] - x2[2] * cs1[1]) * sc; o2[n][2] = (x1[2] * cs1[1] + x2[2] * cs1[0]) * sc;
;                             o1[n][3] = (x1[3] * cs1[2] - x2[3] * cs1[3]) * sc; o2[n][3] = (x1[3] * cs1[3] + x2[3] * cs1[2]) * sc;
.LBB0_1306:
	v_add_u32_e32 v62, 0x90, v156
	v_bfe_u32 v60, v62, 6, 7
	v_cndmask_b32_e64 v60, v171, v60, s[6:7]
	v_lshlrev_b32_e32 v142, 9, v60
	s_andn2_b64 vcc, exec, s[2:3]
	v_lshl_add_u64 v[60:61], v[146:147], 0, v[142:143]
	s_cbranch_vccnz .LBB0_1308
	global_load_dwordx4 v[52:55], v[60:61], off
	global_load_dwordx4 v[56:59], v[60:61], off offset:16
	global_load_dwordx4 v[232:235], v[60:61], off offset:32
	global_load_dwordx4 v[236:239], v[60:61], off offset:48
	s_waitcnt vmcnt(2)
	v_mov_b32_e32 v64, v52
	v_mov_b32_e32 v65, v54
	v_mov_b32_e32 v54, v53
	v_mul_f32_e32 v52, v48, v56
	v_mul_f32_e32 v66, v44, v57
	v_mul_f32_e32 v68, v48, v57
	v_mul_f32_e32 v56, v44, v56
	v_mov_b32_e32 v44, v49
	v_mov_b32_e32 v48, v45
	v_pk_mul_f32 v[70:71], v[42:43], v[54:55]
	v_pk_mul_f32 v[42:43], v[42:43], v[64:65]
	v_pk_mul_f32 v[44:45], v[44:45], v[58:59]
	v_pk_mul_f32 v[48:49], v[48:49], v[58:59]
	v_pk_fma_f32 v[42:43], v[46:47], v[54:55], v[42:43]
	v_mov_b32_e32 v53, v44
	v_mov_b32_e32 v67, v45
	v_mov_b32_e32 v69, v49
	v_mov_b32_e32 v57, v48
	v_pk_fma_f32 v[58:59], v[46:47], v[64:65], v[70:71] neg_lo:[0,0,1] neg_hi:[0,0,1]
	v_pk_mul_f32 v[54:55], v[158:159], v[42:43] op_sel_hi:[0,1]
	v_pk_add_f32 v[42:43], v[52:53], v[66:67] neg_lo:[0,1] neg_hi:[0,1]
	v_pk_add_f32 v[44:45], v[68:69], v[56:57]
	v_pk_mul_f32 v[58:59], v[158:159], v[58:59] op_sel_hi:[0,1]
	v_pk_mul_f32 v[56:57], v[158:159], v[42:43] op_sel_hi:[0,1]
	v_pk_mul_f32 v[52:53], v[158:159], v[44:45] op_sel_hi:[0,1]

;     __device__ __forceinline__ void operator()(const f32x4 (&acc)[2][2][4][2], const Unit& u, int wr, int wc, int fr, int fq) const {
;     ...
;                     for (int n = 0; n < 2; ++n) {
;                         const f32x4 x1 = acc[ai][0][m][n], x2 = acc[ai][1][m][n];
;                         if (lat) { const f32x4 cs0 = tp[2 * n], cs1 = tp[2 * n + 1];
;                             o1[n][0] = (x1[0] * cs0[0] - x2[0] * cs0[1]) * sc; o2[n][0] = (x1[0] * cs0[1] + x2[0] * cs0[0]) * sc;
;                             o1[n][1] = (x1[1] * cs0[2] - x2[1] * cs0[3]) * sc; o2[n][1] = (x1[1] * cs0[3] + x2[1] * cs0[2]) * sc;
;                             o1[n][2] = (x1[2] * cs1[0] - x2[2] * cs1[1]) * sc; o2[n][2] = (x1[2] * cs1[1] + x2[2] * cs1[0]) * sc;
;                             o1[n][3] = (x1[3] * cs1[2] - x2[3] * cs1[3]) * sc; o2[n][3] = (x1[3] * cs1[3] + x2[3] * cs1[2]) * sc;
;                         } else { o1[n] = x1 * sc; o2[n] = x2 * sc; }
.LBB0_1311:
	s_waitcnt vmcnt(0)
	v_mov_b32_e32 v42, v232
	v_mov_b32_e32 v43, v233
	v_mov_b32_e32 v44, v234
	v_mov_b32_e32 v45, v235
	v_mov_b32_e32 v46, v236
	v_mov_b32_e32 v47, v237
	v_mov_b32_e32 v48, v238
	v_mov_b32_e32 v49, v239
	v_mov_b32_e32 v60, v42
	v_mov_b32_e32 v61, v44
	v_mov_b32_e32 v44, v43
	v_mul_f32_e32 v42, v40, v46
	v_mul_f32_e32 v64, v36, v47
	v_mul_f32_e32 v66, v40, v47
	v_mul_f32_e32 v68, v36, v46
	v_mov_b32_e32 v36, v41
	v_mov_b32_e32 v40, v37
	v_pk_mul_f32 v[46:47], v[34:35], v[44:45]
	v_pk_mul_f32 v[34:35], v[34:35], v[60:61]
	v_pk_mul_f32 v[36:37], v[36:37], v[48:49]
	v_pk_mul_f32 v[40:41], v[40:41], v[48:49]
	v_pk_fma_f32 v[46:47], v[38:39], v[60:61], v[46:47] neg_lo:[0,0,1] neg_hi:[0,0,1]
	v_pk_fma_f32 v[34:35], v[38:39], v[44:45], v[34:35]
	v_mov_b32_e32 v43, v36
	v_mov_b32_e32 v65, v37
	v_mov_b32_e32 v67, v41
	v_mov_b32_e32 v69, v40
	v_pk_mul_f32 v[48:49], v[158:159], v[46:47] op_sel_hi:[0,1]
	v_pk_mul_f32 v[46:47], v[158:159], v[34:35] op_sel_hi:[0,1]
	v_pk_add_f32 v[34:35], v[42:43], v[64:65] neg_lo:[0,1] neg_hi:[0,1]
	v_pk_add_f32 v[36:37], v[66:67], v[68:69]
	v_pk_mul_f32 v[42:43], v[158:159], v[34:35] op_sel_hi:[0,1]
	v_pk_mul_f32 v[44:45], v[158:159], v[36:37] op_sel_hi:[0,1]

;     __device__ __forceinline__ void operator()(const f32x4 (&acc)[2][2][4][2], const Unit& u, int wr, int wc, int fr, int fq) const {
;     ...
;                     const int row = row0 + ai * HALF + m * 16; const int t = row & (SEQ - 1);
;                     const int pos = wc < 2 ? (t >> 6) : (t & 63);
;                     const f32x4* tp = (const f32x4*)(rope + pos * 64 + (wc & 1) * 32 + 8 * fq);
;                     f32x4 o1[2], o2[2];
; #pragma unroll
;                     for (int n = 0; n < 2; ++n) {
;                         const f32x4 x1 = acc[ai][0][m][n], x2 = acc[ai][1][m][n];
;                         if (lat) { const f32x4 cs0 = tp[2 * n], cs1 = tp[2 * n + 1];
;                             o1[n][0] = (x1[0] * cs0[0] - x2[0] * cs0[1]) * sc; o2[n][0] = (x1[0] * cs0[1] + x2[0] * cs0[0]) * sc;
;                             o1[n][1] = (x1[1] * cs0[2] - x2[1] * cs0[3]) * sc; o2[n][1] = (x1[1] * cs0[3] + x2[1] * cs0[2]) * sc;
;                             o1[n][2] = (x1[2] * cs1[0] - x2[2] * cs1[1]) * sc; o2[n][2] = (x1[2] * cs1[1] + x2[2] * cs1[0]) * sc;
;                             o1[n][3] = (x1[3] * cs1[2] - x2[3] * cs1[3]) * sc; o2[n][3] = (x1[3] * cs1[3] + x2[3] * cs1[2]) * sc;
.LBB0_1314:
	v_add_u32_e32 v44, 0xa0, v156
	v_bfe_u32 v42, v44, 6, 7
	v_cndmask_b32_e64 v42, v172, v42, s[6:7]
	v_lshlrev_b32_e32 v142, 9, v42
	s_andn2_b64 vcc, exec, s[2:3]
	v_lshl_add_u64 v[42:43], v[146:147], 0, v[142:143]
	s_cbranch_vccnz .LBB0_1316
	global_load_dwordx4 v[34:37], v[42:43], off
	global_load_dwordx4 v[38:41], v[42:43], off offset:16
	global_load_dwordx4 v[232:235], v[42:43], off offset:32
	global_load_dwordx4 v[236:239], v[42:43], off offset:48
	s_waitcnt vmcnt(2)
	v_mov_b32_e32 v46, v34
	v_mov_b32_e32 v47, v36
	v_mov_b32_e32 v36, v35
	v_mul_f32_e32 v34, v32, v38
	v_mul_f32_e32 v48, v28, v39
	v_mul_f32_e32 v52, v32, v39
	v_mul_f32_e32 v38, v28, v38
	v_mov_b32_e32 v28, v33
	v_mov_b32_e32 v32, v29
	v_pk_mul_f32 v[54:55], v[26:27], v[36:37]
	v_pk_mul_f32 v[26:27], v[26:27], v[46:47]
	v_pk_mul_f32 v[28:29], v[28:29], v[40:41]
	v_pk_mul_f32 v[32:33], v[32:33], v[40:41]
	v_pk_fma_f32 v[26:27], v[30:31], v[36:37], v[26:27]
	v_mov_b32_e32 v35, v28
	v_mov_b32_e32 v49, v29
	v_mov_b32_e32 v53, v33
	v_mov_b32_e32 v39, v32
	v_pk_fma_f32 v[40:41], v[30:31], v[46:47], v[54:55] neg_lo:[0,0,1] neg_hi:[0,0,1]
	v_pk_mul_f32 v[36:37], v[158:159], v[26:27] op_sel_hi:[0,1]
	v_pk_add_f32 v[26:27], v[34:35], v[48:49] neg_lo:[0,1] neg_hi:[0,1]
	v_pk_add_f32 v[28:29], v[52:53], v[38:39]
	v_pk_mul_f32 v[40:41], v[158:159], v[40:41] op_sel_hi:[0,1]
	v_pk_mul_f32 v[38:39], v[158:159], v[26:27] op_sel_hi:[0,1]
	v_pk_mul_f32 v[34:35], v[158:159], v[28:29] op_sel_hi:[0,1]

;     __device__ __forceinline__ void operator()(const f32x4 (&acc)[2][2][4][2], const Unit& u, int wr, int wc, int fr, int fq) const {
;     ...
;                         if (lat) { const f32x4 cs0 = tp[2 * n], cs1 = tp[2 * n + 1];
;                             o1[n][0] = (x1[0] * cs0[0] - x2[0] * cs0[1]) * sc; o2[n][0] = (x1[0] * cs0[1] + x2[0] * cs0[0]) * sc;
;                             o1[n][1] = (x1[1] * cs0[2] - x2[1] * cs0[3]) * sc; o2[n][1] = (x1[1] * cs0[3] + x2[1] * cs0[2]) * sc;
;                             o1[n][2] = (x1[2] * cs1[0] - x2[2] * cs1[1]) * sc; o2[n][2] = (x1[2] * cs1[1] + x2[2] * cs1[0]) * sc;
;                             o1[n][3] = (x1[3] * cs1[2] - x2[3] * cs1[3]) * sc; o2[n][3] = (x1[3] * cs1[3] + x2[3] * cs1[2]) * sc;
;                         } else { o1[n] = x1 * sc; o2[n] = x2 * sc; }
.LBB0_1319:
	s_waitcnt vmcnt(0)
	v_mov_b32_e32 v26, v232
	v_mov_b32_e32 v27, v233
	v_mov_b32_e32 v28, v234
	v_mov_b32_e32 v29, v235
	v_mov_b32_e32 v30, v236
	v_mov_b32_e32 v31, v237
	v_mov_b32_e32 v32, v238
	v_mov_b32_e32 v33, v239
	v_mov_b32_e32 v42, v26
	v_mov_b32_e32 v43, v28
	v_mov_b32_e32 v28, v27
	v_mul_f32_e32 v26, v24, v30
	v_mul_f32_e32 v46, v20, v31
	v_mul_f32_e32 v48, v24, v31
	v_mul_f32_e32 v52, v20, v30
	v_mov_b32_e32 v20, v25
	v_mov_b32_e32 v24, v21
	v_pk_mul_f32 v[30:31], v[18:19], v[28:29]
	v_pk_mul_f32 v[18:19], v[18:19], v[42:43]
	v_pk_mul_f32 v[20:21], v[20:21], v[32:33]
	v_pk_mul_f32 v[24:25], v[24:25], v[32:33]
	v_pk_fma_f32 v[30:31], v[22:23], v[42:43], v[30:31] neg_lo:[0,0,1] neg_hi:[0,0,1]
	v_pk_fma_f32 v[18:19], v[22:23], v[28:29], v[18:19]
	v_mov_b32_e32 v27, v20
	v_mov_b32_e32 v47, v21
	v_mov_b32_e32 v49, v25
	v_mov_b32_e32 v53, v24
	v_pk_mul_f32 v[32:33], v[158:159], v[30:31] op_sel_hi:[0,1]
	v_pk_mul_f32 v[30:31], v[158:159], v[18:19] op_sel_hi:[0,1]
	v_pk_add_f32 v[18:19], v[26:27], v[46:47] neg_lo:[0,1] neg_hi:[0,1]
	v_pk_add_f32 v[20:21], v[48:49], v[52:53]
	v_pk_mul_f32 v[26:27], v[158:159], v[18:19] op_sel_hi:[0,1]
	v_pk_mul_f32 v[28:29], v[158:159], v[20:21] op_sel_hi:[0,1]

;     __device__ __forceinline__ void operator()(const f32x4 (&acc)[2][2][4][2], const Unit& u, int wr, int wc, int fr, int fq) const {
;     ...
;                     const int row = row0 + ai * HALF + m * 16; const int t = row & (SEQ - 1);
;                     const int pos = wc < 2 ? (t >> 6) : (t & 63);
;                     const f32x4* tp = (const f32x4*)(rope + pos * 64 + (wc & 1) * 32 + 8 * fq);
;                     f32x4 o1[2], o2[2];
; #pragma unroll
;                     for (int n = 0; n < 2; ++n) {
;                         const f32x4 x1 = acc[ai][0][m][n], x2 = acc[ai][1][m][n];
;                         if (lat) { const f32x4 cs0 = tp[2 * n], cs1 = tp[2 * n + 1];
;                             o1[n][0] = (x1[0] * cs0[0] - x2[0] * cs0[1]) * sc; o2[n][0] = (x1[0] * cs0[1] + x2[0] * cs0[0]) * sc;
;                             o1[n][1] = (x1[1] * cs0[2] - x2[1] * cs0[3]) * sc; o2[n][1] = (x1[1] * cs0[3] + x2[1] * cs0[2]) * sc;
;                             o1[n][2] = (x1[2] * cs1[0] - x2[2] * cs1[1]) * sc; o2[n][2] = (x1[2] * cs1[1] + x2[2] * cs1[0]) * sc;
;                             o1[n][3] = (x1[3] * cs1[2] - x2[3] * cs1[3]) * sc; o2[n][3] = (x1[3] * cs1[3] + x2[3] * cs1[2]) * sc;
;                         } else { o1[n] = x1 * sc; o2[n] = x2 * sc; }
.LBB0_1322:
	v_add_u32_e32 v28, 0xb0, v156
	v_bfe_u32 v26, v28, 6, 7
	v_cndmask_b32_e64 v26, v173, v26, s[6:7]
	v_lshlrev_b32_e32 v142, 9, v26
	s_andn2_b64 vcc, exec, s[2:3]
	v_lshl_add_u64 v[26:27], v[146:147], 0, v[142:143]
	s_cbranch_vccnz .LBB0_1324
	global_load_dwordx4 v[18:21], v[26:27], off
	global_load_dwordx4 v[22:25], v[26:27], off offset:16
	global_load_dwordx4 v[232:235], v[26:27], off offset:32
	global_load_dwordx4 v[236:239], v[26:27], off offset:48
	s_waitcnt vmcnt(2)
	v_mov_b32_e32 v30, v18
	v_mov_b32_e32 v31, v20
	v_mov_b32_e32 v20, v19
	v_mul_f32_e32 v18, v16, v22
	v_mul_f32_e32 v32, v12, v23
	v_mul_f32_e32 v34, v16, v23
	v_mul_f32_e32 v22, v12, v22
	v_mov_b32_e32 v12, v17
	v_mov_b32_e32 v16, v13
	v_pk_mul_f32 v[36:37], v[10:11], v[20:21]
	v_pk_mul_f32 v[10:11], v[10:11], v[30:31]
	v_pk_mul_f32 v[12:13], v[12:13], v[24:25]
	v_pk_mul_f32 v[16:17], v[16:17], v[24:25]
	v_pk_fma_f32 v[10:11], v[14:15], v[20:21], v[10:11]
	v_mov_b32_e32 v19, v12
	v_mov_b32_e32 v33, v13
	v_mov_b32_e32 v35, v17
	v_mov_b32_e32 v23, v16
	v_pk_fma_f32 v[24:25], v[14:15], v[30:31], v[36:37] neg_lo:[0,0,1] neg_hi:[0,0,1]
	v_pk_mul_f32 v[20:21], v[158:159], v[10:11] op_sel_hi:[0,1]
	v_pk_add_f32 v[10:11], v[18:19], v[32:33] neg_lo:[0,1] neg_hi:[0,1]
	v_pk_add_f32 v[12:13], v[34:35], v[22:23]
	v_pk_mul_f32 v[24:25], v[158:159], v[24:25] op_sel_hi:[0,1]
	v_pk_mul_f32 v[22:23], v[158:159], v[10:11] op_sel_hi:[0,1]
	v_pk_mul_f32 v[18:19], v[158:159], v[12:13] op_sel_hi:[0,1]

;     __device__ __forceinline__ void operator()(const f32x4 (&acc)[2][2][4][2], const Unit& u, int wr, int wc, int fr, int fq) const {
;     ...
;                         if (lat) { const f32x4 cs0 = tp[2 * n], cs1 = tp[2 * n + 1];
;                             o1[n][0] = (x1[0] * cs0[0] - x2[0] * cs0[1]) * sc; o2[n][0] = (x1[0] * cs0[1] + x2[0] * cs0[0]) * sc;
;                             o1[n][1] = (x1[1] * cs0[2] - x2[1] * cs0[3]) * sc; o2[n][1] = (x1[1] * cs0[3] + x2[1] * cs0[2]) * sc;
;                             o1[n][2] = (x1[2] * cs1[0] - x2[2] * cs1[1]) * sc; o2[n][2] = (x1[2] * cs1[1] + x2[2] * cs1[0]) * sc;
;                             o1[n][3] = (x1[3] * cs1[2] - x2[3] * cs1[3]) * sc; o2[n][3] = (x1[3] * cs1[3] + x2[3] * cs1[2]) * sc;
;                         } else { o1[n] = x1 * sc; o2[n] = x2 * sc; }
.LBB0_1327:
	s_waitcnt vmcnt(0)
	v_mov_b32_e32 v10, v232
	v_mov_b32_e32 v11, v233
	v_mov_b32_e32 v12, v234
	v_mov_b32_e32 v13, v235
	v_mov_b32_e32 v14, v236
	v_mov_b32_e32 v15, v237
	v_mov_b32_e32 v16, v238
	v_mov_b32_e32 v17, v239
	v_mov_b32_e32 v26, v10
	v_mov_b32_e32 v27, v12
	v_mov_b32_e32 v12, v11
	v_mul_f32_e32 v10, v8, v14
	v_mul_f32_e32 v30, v4, v15
	v_mul_f32_e32 v32, v8, v15
	v_mul_f32_e32 v34, v4, v14
	v_mov_b32_e32 v4, v9
	v_mov_b32_e32 v8, v5
	v_pk_mul_f32 v[14:15], v[2:3], v[12:13]
	v_pk_mul_f32 v[2:3], v[2:3], v[26:27]
	v_pk_mul_f32 v[4:5], v[4:5], v[16:17]
	v_pk_mul_f32 v[8:9], v[8:9], v[16:17]
	v_pk_fma_f32 v[14:15], v[6:7], v[26:27], v[14:15] neg_lo:[0,0,1] neg_hi:[0,0,1]
	v_pk_fma_f32 v[2:3], v[6:7], v[12:13], v[2:3]
	v_mov_b32_e32 v11, v4
	v_mov_b32_e32 v31, v5
	v_mov_b32_e32 v33, v9
	v_mov_b32_e32 v35, v8
	v_pk_mul_f32 v[16:17], v[158:159], v[14:15] op_sel_hi:[0,1]
	v_pk_mul_f32 v[14:15], v[158:159], v[2:3] op_sel_hi:[0,1]
	v_pk_add_f32 v[2:3], v[10:11], v[30:31] neg_lo:[0,1] neg_hi:[0,1]
	v_pk_add_f32 v[4:5], v[32:33], v[34:35]
	v_pk_mul_f32 v[10:11], v[158:159], v[2:3] op_sel_hi:[0,1]
	v_pk_mul_f32 v[12:13], v[158:159], v[4:5] op_sel_hi:[0,1]
